# speedup vs baseline: 1.0026x; 1.0026x over previous
_Z16sum_layer_kernelPKfS0_Pf:
	s_load_dwordx4 s[4:7], s[0:1], 0x0
	s_load_dwordx2 s[8:9], s[0:1], 0x10
	s_cmp_lt_u32 s2, 0x100
	s_cbranch_scc1 .Lskip_late_sleep
	s_sleep 32
.Lskip_late_sleep:
	v_lshrrev_b32_e32 v42, 6, v0
	v_bfe_u32 v41, v0, 5, 1
	v_and_b32_e32 v40, 31, v0
	v_readfirstlane_b32 s23, v42
	v_and_b32_e32 v43, 7, v0
	v_bfe_u32 v44, v0, 3, 3
	s_lshl_b32 s3, s2, 12
	s_lshl_b32 s19, s2, 7
	s_lshl_b32 s23, s23, 12
	v_lshlrev_b32_e32 v1, 11, v41
	v_lshl_or_b32 v1, v40, 2, v1
	s_mov_b32 m0, s23
	v_lshrrev_b32_e32 v46, 1, v44
	v_xor_b32_e32 v46, v43, v46
	v_lshlrev_b32_e32 v46, 4, v46
	v_lshl_add_u32 v35, v44, 16, v46
	v_lshl_add_u32 v35, v42, 21, v35
	v_add_u32_e32 v35, s19, v35
	v_xor_b32_e32 v86, 64, v35
	s_mov_b32 s20, 0x7fc00
	s_mov_b32 s21, 0xff800
	s_mov_b32 s22, 0x17f400
	s_mov_b32 s14, 0x200000
	s_mov_b32 s15, 0x20000
	s_waitcnt lgkmcnt(0)
	s_mov_b32 s12, s6
	s_and_b32 s13, s7, 0xffff
	s_and_b32 s5, s5, 0xffff
	s_mov_b32 s6, 0x800000
	s_mov_b32 s7, s15
	buffer_load_dword v18, v1, s[12:15], s3 offen nt
	buffer_load_dword v19, v1, s[12:15], s3 offen offset:128 nt
	buffer_load_dword v20, v1, s[12:15], s3 offen offset:256 nt
	buffer_load_dword v21, v1, s[12:15], s3 offen offset:384 nt
	buffer_load_dword v22, v1, s[12:15], s3 offen offset:512 nt
	buffer_load_dword v23, v1, s[12:15], s3 offen offset:640 nt
	buffer_load_dword v24, v1, s[12:15], s3 offen offset:768 nt
	buffer_load_dword v25, v1, s[12:15], s3 offen offset:896 nt
	buffer_load_dword v26, v1, s[12:15], s3 offen offset:1024 nt
	buffer_load_dword v27, v1, s[12:15], s3 offen offset:1152 nt
	buffer_load_dword v28, v1, s[12:15], s3 offen offset:1280 nt
	buffer_load_dword v29, v1, s[12:15], s3 offen offset:1408 nt
	buffer_load_dword v30, v1, s[12:15], s3 offen offset:1536 nt
	buffer_load_dword v31, v1, s[12:15], s3 offen offset:1664 nt
	buffer_load_dword v32, v1, s[12:15], s3 offen offset:1792 nt
	buffer_load_dword v33, v1, s[12:15], s3 offen offset:1920 nt
	buffer_load_dwordx4 v35, s[4:7], 0 offen nt lds
	buffer_load_dwordx4 v86, s[4:7], s20 offen offset:1024 nt lds
	buffer_load_dwordx4 v35, s[4:7], s21 offen offset:2048 nt lds
	buffer_load_dwordx4 v86, s[4:7], s22 offen offset:3072 nt lds
	v_and_b32_e32 v45, 63, v0
	v_lshlrev_b32_e32 v36, 2, v40
	v_lshl_add_u32 v36, v41, 18, v36
	v_lshl_add_u32 v36, v42, 21, v36
	v_add_u32_e32 v36, s19, v36
	v_bfe_u32 v47, v40, 1, 3
	v_lshlrev_b32_e32 v39, 2, v41
	v_xor_b32_e32 v39, v39, v47
	v_lshlrev_b32_e32 v39, 4, v39
	v_lshl_add_u32 v39, v40, 7, v39
	v_lshl_add_u32 v39, v42, 12, v39
	v_xor_b32_e32 v81, 16, v39
	v_xor_b32_e32 v82, 32, v39
	v_xor_b32_e32 v83, 48, v39
	v_cmp_gt_u32_e32 vcc, 32, v45
	v_mov_b32_e32 v34, 0xc1600000
	v_mov_b32_e32 v84, 0x3fb8aa3b
	v_mov_b32_e32 v85, 0x3f317218
	s_lshl_b32 s24, 1, 16
	s_lshl_b32 s25, 2, 16
	s_lshl_b32 s26, 3, 16
	s_lshl_b32 s27, 8, 16
	s_lshl_b32 s28, 9, 16
	s_lshl_b32 s29, 10, 16
	s_lshl_b32 s30, 11, 16
	s_lshl_b32 s31, 16, 16
	s_lshl_b32 s32, 17, 16
	s_lshl_b32 s33, 18, 16
	s_lshl_b32 s34, 19, 16
	s_lshl_b32 s35, 24, 16
	s_lshl_b32 s36, 25, 16
	s_lshl_b32 s37, 26, 16
	s_lshl_b32 s38, 27, 16
	s_and_b32 s9, s9, 0xffff
	s_mov_b32 s10, s6
	s_mov_b32 s11, s15
	s_waitcnt vmcnt(4)
	v_max3_f32 v48, v18, v19, v20
	v_max3_f32 v50, v21, v22, v23
	v_max3_f32 v48, v48, v24, v25
	v_max3_f32 v50, v50, v26, v27
	v_max3_f32 v48, v48, v28, v29
	v_max3_f32 v50, v50, v30, v31
	v_max3_f32 v48, v48, v32, v33
	v_max_f32_e32 v48, v48, v50
	v_mov_b32_e32 v50, v48
	s_nop 1
	v_permlane32_swap_b32_e32 v48, v50
	v_max_f32_e32 v48, v48, v50
	v_fmamk_f32 v48, v48, 0x3fb8aa3b, v34
	v_pk_fma_f32 v[18:19], v[18:19], v[84:85], v[48:49] op_sel_hi:[1,0,0] neg_lo:[0,0,1] neg_hi:[0,0,1]
	v_exp_f32_e32 v18, v18
	v_exp_f32_e32 v19, v19
	v_pk_fma_f32 v[20:21], v[20:21], v[84:85], v[48:49] op_sel_hi:[1,0,0] neg_lo:[0,0,1] neg_hi:[0,0,1]
	v_exp_f32_e32 v20, v20
	v_exp_f32_e32 v21, v21
	v_pk_fma_f32 v[22:23], v[22:23], v[84:85], v[48:49] op_sel_hi:[1,0,0] neg_lo:[0,0,1] neg_hi:[0,0,1]
	v_exp_f32_e32 v22, v22
	v_exp_f32_e32 v23, v23
	v_pk_fma_f32 v[24:25], v[24:25], v[84:85], v[48:49] op_sel_hi:[1,0,0] neg_lo:[0,0,1] neg_hi:[0,0,1]
	v_exp_f32_e32 v24, v24
	v_exp_f32_e32 v25, v25
	v_pk_fma_f32 v[26:27], v[26:27], v[84:85], v[48:49] op_sel_hi:[1,0,0] neg_lo:[0,0,1] neg_hi:[0,0,1]
	v_exp_f32_e32 v26, v26
	v_exp_f32_e32 v27, v27
	v_pk_fma_f32 v[28:29], v[28:29], v[84:85], v[48:49] op_sel_hi:[1,0,0] neg_lo:[0,0,1] neg_hi:[0,0,1]
	v_exp_f32_e32 v28, v28
	v_exp_f32_e32 v29, v29
	v_pk_fma_f32 v[30:31], v[30:31], v[84:85], v[48:49] op_sel_hi:[1,0,0] neg_lo:[0,0,1] neg_hi:[0,0,1]
	v_exp_f32_e32 v30, v30
	v_exp_f32_e32 v31, v31
	v_pk_fma_f32 v[32:33], v[32:33], v[84:85], v[48:49] op_sel_hi:[1,0,0] neg_lo:[0,0,1] neg_hi:[0,0,1]
	v_exp_f32_e32 v32, v32
	v_exp_f32_e32 v33, v33
	v_pk_add_f32 v[56:57], v[18:19], v[20:21]
	v_pk_add_f32 v[58:59], v[22:23], v[24:25]
	v_pk_add_f32 v[60:61], v[26:27], v[28:29]
	v_pk_add_f32 v[62:63], v[30:31], v[32:33]
	v_pk_add_f32 v[56:57], v[56:57], v[58:59]
	v_pk_add_f32 v[60:61], v[60:61], v[62:63]
	v_pk_add_f32 v[56:57], v[56:57], v[60:61]
	v_add_f32_e32 v50, v56, v57
	v_mov_b32_e32 v51, v50
	s_nop 1
	v_permlane32_swap_b32_e32 v50, v51
	v_add_f32_e32 v50, v50, v51
	v_log_f32_e32 v50, v50
	v_cvt_pk_f16_f32 v40, v18, v19
	v_cvt_pk_f16_f32 v41, v20, v21
	v_cvt_pk_f16_f32 v42, v22, v23
	v_cvt_pk_f16_f32 v43, v24, v25
	v_cvt_pk_f16_f32 v44, v26, v27
	v_cvt_pk_f16_f32 v45, v28, v29
	v_cvt_pk_f16_f32 v46, v30, v31
	v_cvt_pk_f16_f32 v47, v32, v33
	v_add_f32_e32 v50, 0x41600000, v50
	v_mul_f32_e32 v50, 0xbf317218, v50
	v_cndmask_b32_e64 v51, v50, 1.0, vcc
	s_waitcnt vmcnt(0)
	ds_read_b128 v[2:5], v39
	ds_read_b128 v[6:9], v81
	ds_read_b128 v[10:13], v82
	ds_read_b128 v[14:17], v83
	s_waitcnt lgkmcnt(2)
	v_max3_f32 v52, v2, v3, v4
	v_max3_f32 v53, v5, v6, v7
	v_max_f32_e32 v52, v52, v8
	v_max_f32_e32 v53, v53, v9
	s_waitcnt lgkmcnt(0)
	v_max3_f32 v52, v52, v10, v11
	v_max3_f32 v53, v53, v12, v13
	v_max3_f32 v52, v52, v14, v15
	v_max3_f32 v53, v53, v16, v17
	v_max_f32_e32 v52, v52, v53
	v_mov_b32_e32 v53, v52
	s_nop 1
	v_permlane32_swap_b32_e32 v52, v53
	v_max_f32_e32 v52, v52, v53
	v_cndmask_b32_e32 v54, 1.0, v52, vcc
	v_fmamk_f32 v48, v52, 0x3fb8aa3b, v34
	v_pk_fma_f32 v[2:3], v[2:3], v[84:85], v[48:49] op_sel_hi:[1,0,0] neg_lo:[0,0,1] neg_hi:[0,0,1]
	v_mfma_f32_32x32x2_f32 v[64:79], v54, v51, 0
	v_exp_f32_e32 v2, v2
	v_exp_f32_e32 v3, v3
	v_pk_fma_f32 v[4:5], v[4:5], v[84:85], v[48:49] op_sel_hi:[1,0,0] neg_lo:[0,0,1] neg_hi:[0,0,1]
	v_exp_f32_e32 v4, v4
	v_exp_f32_e32 v5, v5
	v_pk_fma_f32 v[6:7], v[6:7], v[84:85], v[48:49] op_sel_hi:[1,0,0] neg_lo:[0,0,1] neg_hi:[0,0,1]
	v_exp_f32_e32 v6, v6
	v_exp_f32_e32 v7, v7
	v_pk_fma_f32 v[8:9], v[8:9], v[84:85], v[48:49] op_sel_hi:[1,0,0] neg_lo:[0,0,1] neg_hi:[0,0,1]
	v_exp_f32_e32 v8, v8
	v_exp_f32_e32 v9, v9
	v_pk_fma_f32 v[10:11], v[10:11], v[84:85], v[48:49] op_sel_hi:[1,0,0] neg_lo:[0,0,1] neg_hi:[0,0,1]
	v_exp_f32_e32 v10, v10
	v_cvt_pk_f16_f32 v56, v2, v3
	v_cvt_pk_f16_f32 v57, v4, v5
	v_cvt_pk_f16_f32 v58, v6, v7
	v_cvt_pk_f16_f32 v59, v8, v9
	v_exp_f32_e32 v11, v11
	v_pk_fma_f32 v[12:13], v[12:13], v[84:85], v[48:49] op_sel_hi:[1,0,0] neg_lo:[0,0,1] neg_hi:[0,0,1]
	v_exp_f32_e32 v12, v12
	v_mfma_f32_32x32x16_f16 v[18:33], v[56:59], v[40:43], 0
	v_exp_f32_e32 v13, v13
	v_pk_fma_f32 v[14:15], v[14:15], v[84:85], v[48:49] op_sel_hi:[1,0,0] neg_lo:[0,0,1] neg_hi:[0,0,1]
	v_exp_f32_e32 v14, v14
	v_exp_f32_e32 v15, v15
	v_pk_fma_f32 v[16:17], v[16:17], v[84:85], v[48:49] op_sel_hi:[1,0,0] neg_lo:[0,0,1] neg_hi:[0,0,1]
	v_exp_f32_e32 v16, v16
	v_exp_f32_e32 v17, v17
	v_cvt_pk_f16_f32 v60, v10, v11
	v_cvt_pk_f16_f32 v61, v12, v13
	v_cvt_pk_f16_f32 v62, v14, v15
	v_cvt_pk_f16_f32 v63, v16, v17
	s_nop 1
	v_mfma_f32_32x32x16_f16 v[18:33], v[60:63], v[44:47], v[18:33]
	s_nop 11
	v_log_f32_e32 v18, v18
	v_log_f32_e32 v19, v19
	v_log_f32_e32 v20, v20
	v_log_f32_e32 v21, v21
	v_log_f32_e32 v22, v22
	v_log_f32_e32 v23, v23
	v_pk_fma_f32 v[64:65], v[18:19], v[84:85], v[64:65] op_sel:[0,1,0] op_sel_hi:[1,1,1]
	buffer_store_dword v64, v36, s[8:11], 0 offen
	buffer_store_dword v65, v36, s[8:11], s24 offen
	v_log_f32_e32 v24, v24
	v_log_f32_e32 v25, v25
	v_pk_fma_f32 v[66:67], v[20:21], v[84:85], v[66:67] op_sel:[0,1,0] op_sel_hi:[1,1,1]
	buffer_store_dword v66, v36, s[8:11], s25 offen
	buffer_store_dword v67, v36, s[8:11], s26 offen
	v_log_f32_e32 v26, v26
	v_log_f32_e32 v27, v27
	v_pk_fma_f32 v[68:69], v[22:23], v[84:85], v[68:69] op_sel:[0,1,0] op_sel_hi:[1,1,1]
	buffer_store_dword v68, v36, s[8:11], s27 offen
	buffer_store_dword v69, v36, s[8:11], s28 offen
	v_log_f32_e32 v28, v28
	v_log_f32_e32 v29, v29
	v_pk_fma_f32 v[70:71], v[24:25], v[84:85], v[70:71] op_sel:[0,1,0] op_sel_hi:[1,1,1]
	buffer_store_dword v70, v36, s[8:11], s29 offen
	buffer_store_dword v71, v36, s[8:11], s30 offen
	v_log_f32_e32 v30, v30
	v_log_f32_e32 v31, v31
	v_pk_fma_f32 v[72:73], v[26:27], v[84:85], v[72:73] op_sel:[0,1,0] op_sel_hi:[1,1,1]
	buffer_store_dword v72, v36, s[8:11], s31 offen
	buffer_store_dword v73, v36, s[8:11], s32 offen
	v_log_f32_e32 v32, v32
	v_log_f32_e32 v33, v33
	v_pk_fma_f32 v[74:75], v[28:29], v[84:85], v[74:75] op_sel:[0,1,0] op_sel_hi:[1,1,1]
	buffer_store_dword v74, v36, s[8:11], s33 offen
	buffer_store_dword v75, v36, s[8:11], s34 offen
	v_pk_fma_f32 v[76:77], v[30:31], v[84:85], v[76:77] op_sel:[0,1,0] op_sel_hi:[1,1,1]
	buffer_store_dword v76, v36, s[8:11], s35 offen
	buffer_store_dword v77, v36, s[8:11], s36 offen
	v_pk_fma_f32 v[78:79], v[32:33], v[84:85], v[78:79] op_sel:[0,1,0] op_sel_hi:[1,1,1]
	buffer_store_dword v78, v36, s[8:11], s37 offen
	buffer_store_dword v79, v36, s[8:11], s38 offen
	s_endpgm
